# baseline (speedup 1.0000x reference)
.LBB4_1:
	v_lshl_add_u64 v[30:31], v[0:1], 0, s[2:3]
	ds_read_b128 v[2:5], v38
	ds_read_b128 v[6:9], v38 offset:1024
	global_load_dwordx4 v[10:13], v[30:31], off
	v_add_co_u32_e32 v34, vcc, s17, v30
	s_add_u32 s2, s2, 0x1000
	s_nop 0
	v_addc_co_u32_e32 v35, vcc, 0, v31, vcc
	v_add_co_u32_e32 v40, vcc, s18, v30
	s_addc_u32 s3, s3, 0
	s_nop 0
	v_addc_co_u32_e32 v41, vcc, 0, v31, vcc
	v_add_co_u32_e32 v46, vcc, s19, v30
	s_cmpk_eq_i32 s2, 0x4000
	s_nop 0
	v_addc_co_u32_e32 v47, vcc, 0, v31, vcc
	global_load_dwordx4 v[14:17], v[30:31], off offset:1024
	global_load_dwordx4 v[18:21], v[34:35], off
	global_load_dwordx4 v[22:25], v[40:41], off
	global_load_dwordx4 v[26:29], v[46:47], off
	s_waitcnt vmcnt(2) lgkmcnt(1)
	v_mfma_f32_32x32x16_f16 a[16:31], v[18:21], v[2:5], a[16:31]
	global_load_dwordx4 v[18:21], v[40:41], off offset:1024
	v_mfma_f32_32x32x16_f16 a[0:15], v[10:13], v[2:5], a[0:15]
	global_load_dwordx4 v[10:13], v[34:35], off offset:1024
	s_waitcnt vmcnt(3)
	v_mfma_f32_32x32x16_f16 a[32:47], v[22:25], v[2:5], a[32:47]
	global_load_dwordx4 v[22:25], v[46:47], off offset:1024
	s_waitcnt vmcnt(3)
	v_mfma_f32_32x32x16_f16 a[48:63], v[26:29], v[2:5], a[48:63]
	ds_read_b128 v[2:5], v38 offset:2048
	ds_read_b128 v[26:29], v38 offset:3072
	v_add_u32_e32 v38, 0x1000, v38
	s_waitcnt lgkmcnt(2)
	v_mfma_f32_32x32x16_f16 a[0:15], v[14:17], v[6:9], a[0:15]
	global_load_dwordx4 v[14:17], v[30:31], off offset:2048
	s_nop 0
	global_load_dwordx4 v[30:33], v[30:31], off offset:3072
	s_waitcnt vmcnt(3)
	v_mfma_f32_32x32x16_f16 a[16:31], v[10:13], v[6:9], a[16:31]
	global_load_dwordx4 v[10:13], v[34:35], off offset:2048
	v_mfma_f32_32x32x16_f16 a[32:47], v[18:21], v[6:9], a[32:47]
	global_load_dwordx4 v[18:21], v[40:41], off offset:2048
	s_waitcnt vmcnt(4)
	v_mfma_f32_32x32x16_f16 a[48:63], v[22:25], v[6:9], a[48:63]
	global_load_dwordx4 v[6:9], v[46:47], off offset:2048
	s_waitcnt vmcnt(4) lgkmcnt(1)
	v_mfma_f32_32x32x16_f16 a[0:15], v[14:17], v[2:5], a[0:15]
	global_load_dwordx4 v[14:17], v[34:35], off offset:3072
	s_waitcnt vmcnt(4) lgkmcnt(0)
	v_mfma_f32_32x32x16_f16 a[0:15], v[30:33], v[26:29], a[0:15]
	s_waitcnt vmcnt(3)
	v_mfma_f32_32x32x16_f16 a[16:31], v[10:13], v[2:5], a[16:31]
	global_load_dwordx4 v[10:13], v[40:41], off offset:3072
	s_waitcnt vmcnt(3)
	v_mfma_f32_32x32x16_f16 a[32:47], v[18:21], v[2:5], a[32:47]
	global_load_dwordx4 v[18:21], v[46:47], off offset:3072
	s_waitcnt vmcnt(3)
	v_mfma_f32_32x32x16_f16 a[48:63], v[6:9], v[2:5], a[48:63]
	s_waitcnt vmcnt(2)
	v_mfma_f32_32x32x16_f16 a[16:31], v[14:17], v[26:29], a[16:31]
	s_waitcnt vmcnt(1)
	v_mfma_f32_32x32x16_f16 a[32:47], v[10:13], v[26:29], a[32:47]
	s_waitcnt vmcnt(0)
	v_mfma_f32_32x32x16_f16 a[48:63], v[18:21], v[26:29], a[48:63]
	s_cbranch_scc0 .LBB4_1
	s_load_dword s3, s[10:11], 0x0
	v_mov_b32_e32 v0, 0xbfb8aa3b
	v_mov_b32_e32 v1, 0
	v_accvgpr_read_b32 v138, a0
	s_add_u32 s2, s14, 0x2000000
	s_waitcnt lgkmcnt(0)
	v_mul_f32_e32 v0, s3, v0
	v_exp_f32_e32 v10, v0
	v_or_b32_e32 v0, v107, v49
	v_lshl_add_u64 v[144:145], s[0:1], 0, v[0:1]
	v_lshlrev_b64 v[144:145], 12, v[144:145]
	v_add_f32_e32 v10, 1.0, v10
	v_div_scale_f32 v11, s[4:5], v10, v10, 1.0
	v_rcp_f32_e32 v32, v11
	v_div_scale_f32 v38, vcc, 1.0, v10, 1.0
	v_or3_b32 v149, v145, 0, 0
	v_fma_f32 v107, -v11, v32, 1.0
	v_fmac_f32_e32 v32, v107, v32
	v_mul_f32_e32 v107, v38, v32
	v_fma_f32 v139, -v11, v107, v38
	v_fmac_f32_e32 v107, v139, v32
	v_fma_f32 v11, -v11, v107, v38
	v_div_fmas_f32 v11, v11, v32, v107
	v_lshlrev_b32_e32 v32, 2, v0
	ds_read_b128 v[140:143], v32 offset:16384
	v_or3_b32 v148, v144, v36, s16
	s_addc_u32 s3, s15, 0
	ds_read_b128 v[144:147], v32 offset:16416
	v_div_fixup_f32 v11, v11, v10, 1.0
	s_waitcnt lgkmcnt(1)
	v_add_f32_e32 v38, v138, v140
	v_lshlrev_b64 v[138:139], 2, v[148:149]
	v_lshl_add_u64 v[148:149], s[14:15], 0, v[138:139]
	v_lshl_add_u64 v[138:139], s[2:3], 0, v[138:139]
	global_store_dword v[138:139], v38, off sc1
	v_or_b32_e32 v138, 1, v0
	v_mov_b32_e32 v139, v1
	v_lshl_add_u64 v[138:139], s[0:1], 0, v[138:139]
	v_lshlrev_b64 v[138:139], 12, v[138:139]
	v_or3_b32 v139, v139, 0, 0
	v_or3_b32 v138, v138, v36, s16
	v_accvgpr_read_b32 v137, a1
	v_sub_f32_e32 v10, 1.0, v11
	v_mul_f32_e32 v107, v11, v38
	v_lshlrev_b64 v[138:139], 2, v[138:139]
	v_fmac_f32_e32 v107, v10, v112
	v_add_f32_e32 v38, v137, v141
	v_lshl_add_u64 v[140:141], s[14:15], 0, v[138:139]
	v_lshl_add_u64 v[138:139], s[2:3], 0, v[138:139]
	global_store_dword v[148:149], v107, off sc1
	global_store_dword v[138:139], v38, off sc1
	v_or_b32_e32 v138, 2, v0
	v_mov_b32_e32 v139, v1
	v_accvgpr_read_b32 v136, a2
	v_mul_f32_e32 v107, v11, v38
	v_lshl_add_u64 v[138:139], s[0:1], 0, v[138:139]
	v_fmac_f32_e32 v107, v10, v111
	v_lshlrev_b64 v[138:139], 12, v[138:139]
	v_add_f32_e32 v38, v136, v142
	global_store_dword v[140:141], v107, off sc1
	v_or3_b32 v139, v139, 0, 0
	v_or3_b32 v138, v138, v36, s16
	v_mul_f32_e32 v107, v11, v38
	v_fmac_f32_e32 v107, v10, v110
	v_lshlrev_b64 v[110:111], 2, v[138:139]
	v_lshl_add_u64 v[136:137], s[14:15], 0, v[110:111]
	v_lshl_add_u64 v[110:111], s[2:3], 0, v[110:111]
	global_store_dword v[110:111], v38, off sc1
	v_or_b32_e32 v110, 3, v0
	v_mov_b32_e32 v111, v1
	v_lshl_add_u64 v[110:111], s[0:1], 0, v[110:111]
	v_lshlrev_b64 v[110:111], 12, v[110:111]
	v_or3_b32 v111, v111, 0, 0
	v_or3_b32 v110, v110, v36, s16
	v_accvgpr_read_b32 v135, a3
	v_lshlrev_b64 v[110:111], 2, v[110:111]
	global_store_dword v[136:137], v107, off sc1
	v_add_f32_e32 v38, v135, v143
	v_lshl_add_u64 v[136:137], s[14:15], 0, v[110:111]
	v_lshl_add_u64 v[110:111], s[2:3], 0, v[110:111]
	global_store_dword v[110:111], v38, off sc1
	v_or_b32_e32 v110, 8, v0
	v_mov_b32_e32 v111, v1
	v_accvgpr_read_b32 v134, a4
	v_mul_f32_e32 v107, v11, v38
	v_lshl_add_u64 v[110:111], s[0:1], 0, v[110:111]
	v_fmac_f32_e32 v107, v10, v109
	v_lshlrev_b64 v[110:111], 12, v[110:111]
	s_waitcnt lgkmcnt(0)
	v_add_f32_e32 v38, v134, v144
	global_store_dword v[136:137], v107, off sc1
	v_or3_b32 v111, v111, 0, 0
	v_or3_b32 v110, v110, v36, s16
	v_mul_f32_e32 v107, v11, v38
	v_fmac_f32_e32 v107, v10, v108
	v_lshlrev_b64 v[108:109], 2, v[110:111]
	v_lshl_add_u64 v[110:111], s[14:15], 0, v[108:109]
	v_lshl_add_u64 v[108:109], s[2:3], 0, v[108:109]
	global_store_dword v[108:109], v38, off sc1
	v_or_b32_e32 v108, 9, v0
	v_mov_b32_e32 v109, v1
	v_accvgpr_read_b32 v133, a5
	v_lshl_add_u64 v[108:109], s[0:1], 0, v[108:109]
	v_lshlrev_b64 v[108:109], 12, v[108:109]
	v_add_f32_e32 v38, v133, v145
	global_store_dword v[110:111], v107, off sc1
	v_or3_b32 v109, v109, 0, 0
	v_or3_b32 v108, v108, v36, s16
	v_mul_f32_e32 v110, v11, v38
	v_fmac_f32_e32 v110, v10, v106
	v_lshlrev_b64 v[106:107], 2, v[108:109]
	v_lshl_add_u64 v[108:109], s[14:15], 0, v[106:107]
	v_lshl_add_u64 v[106:107], s[2:3], 0, v[106:107]
	global_store_dword v[106:107], v38, off sc1
	v_or_b32_e32 v106, 10, v0
	v_mov_b32_e32 v107, v1
	v_lshl_add_u64 v[106:107], s[0:1], 0, v[106:107]
	v_lshlrev_b64 v[106:107], 12, v[106:107]
	v_or3_b32 v107, v107, 0, 0
	v_or3_b32 v106, v106, v36, s16
	v_accvgpr_read_b32 v132, a6
	v_lshlrev_b64 v[106:107], 2, v[106:107]
	global_store_dword v[108:109], v110, off sc1
	v_add_f32_e32 v38, v132, v146
	v_lshl_add_u64 v[108:109], s[14:15], 0, v[106:107]
	v_lshl_add_u64 v[106:107], s[2:3], 0, v[106:107]
	global_store_dword v[106:107], v38, off sc1
	v_or_b32_e32 v106, 11, v0
	v_mov_b32_e32 v107, v1
	v_accvgpr_read_b32 v131, a7
	v_mul_f32_e32 v110, v11, v38
	v_lshl_add_u64 v[106:107], s[0:1], 0, v[106:107]
	v_fmac_f32_e32 v110, v10, v105
	v_lshlrev_b64 v[106:107], 12, v[106:107]
	v_add_f32_e32 v38, v131, v147
	global_store_dword v[108:109], v110, off sc1
	v_or3_b32 v107, v107, 0, 0
	v_or3_b32 v106, v106, v36, s16
	v_mul_f32_e32 v108, v11, v38
	v_fmac_f32_e32 v108, v10, v104
	v_lshlrev_b64 v[104:105], 2, v[106:107]
	v_lshl_add_u64 v[106:107], s[14:15], 0, v[104:105]
	v_lshl_add_u64 v[104:105], s[2:3], 0, v[104:105]
	global_store_dword v[104:105], v38, off sc1
	v_or_b32_e32 v104, 16, v0
	v_mov_b32_e32 v105, v1
	global_store_dword v[106:107], v108, off sc1
	v_lshl_add_u64 v[108:109], s[0:1], 0, v[104:105]
	ds_read_b128 v[104:107], v32 offset:16448
	v_lshlrev_b64 v[108:109], 12, v[108:109]
	v_accvgpr_read_b32 v130, a8
	v_or3_b32 v133, v109, 0, 0
	v_or3_b32 v132, v108, v36, s16
	ds_read_b128 v[108:111], v32 offset:16480
	s_waitcnt lgkmcnt(1)
	v_add_f32_e32 v38, v130, v104
	v_lshlrev_b64 v[130:131], 2, v[132:133]
	v_lshl_add_u64 v[132:133], s[14:15], 0, v[130:131]
	v_lshl_add_u64 v[130:131], s[2:3], 0, v[130:131]
	global_store_dword v[130:131], v38, off sc1
	v_or_b32_e32 v130, 17, v0
	v_mov_b32_e32 v131, v1
	v_accvgpr_read_b32 v129, a9
	v_lshl_add_u64 v[130:131], s[0:1], 0, v[130:131]
	v_mul_f32_e32 v104, v11, v38
	v_lshlrev_b64 v[130:131], 12, v[130:131]
	v_add_f32_e32 v38, v129, v105
	v_or3_b32 v131, v131, 0, 0
	v_or3_b32 v130, v130, v36, s16
	v_mul_f32_e32 v112, v11, v38
	v_fmac_f32_e32 v104, v10, v103
	v_fmac_f32_e32 v112, v10, v102
	v_lshlrev_b64 v[102:103], 2, v[130:131]
	global_store_dword v[132:133], v104, off sc1
	v_lshl_add_u64 v[104:105], s[14:15], 0, v[102:103]
	v_lshl_add_u64 v[102:103], s[2:3], 0, v[102:103]
	global_store_dword v[102:103], v38, off sc1
	v_or_b32_e32 v102, 18, v0
	v_mov_b32_e32 v103, v1
	v_lshl_add_u64 v[102:103], s[0:1], 0, v[102:103]
	v_lshlrev_b64 v[102:103], 12, v[102:103]
	v_or3_b32 v103, v103, 0, 0
	v_or3_b32 v102, v102, v36, s16
	v_accvgpr_read_b32 v128, a10
	v_lshlrev_b64 v[102:103], 2, v[102:103]
	global_store_dword v[104:105], v112, off sc1
	v_add_f32_e32 v38, v128, v106
	v_lshl_add_u64 v[104:105], s[14:15], 0, v[102:103]
	v_lshl_add_u64 v[102:103], s[2:3], 0, v[102:103]
	global_store_dword v[102:103], v38, off sc1
	v_or_b32_e32 v102, 19, v0
	v_mov_b32_e32 v103, v1
	v_accvgpr_read_b32 v127, a11
	v_mul_f32_e32 v106, v11, v38
	v_lshl_add_u64 v[102:103], s[0:1], 0, v[102:103]
	v_fmac_f32_e32 v106, v10, v101
	v_lshlrev_b64 v[102:103], 12, v[102:103]
	v_add_f32_e32 v38, v127, v107
	global_store_dword v[104:105], v106, off sc1
	v_or3_b32 v103, v103, 0, 0
	v_or3_b32 v102, v102, v36, s16
	v_mul_f32_e32 v104, v11, v38
	v_fmac_f32_e32 v104, v10, v100
	v_lshlrev_b64 v[100:101], 2, v[102:103]
	v_lshl_add_u64 v[102:103], s[14:15], 0, v[100:101]
	v_lshl_add_u64 v[100:101], s[2:3], 0, v[100:101]
	global_store_dword v[100:101], v38, off sc1
	v_or_b32_e32 v100, 24, v0
	v_mov_b32_e32 v101, v1
	v_lshl_add_u64 v[100:101], s[0:1], 0, v[100:101]
	v_lshlrev_b64 v[100:101], 12, v[100:101]
	v_or3_b32 v101, v101, 0, 0
	v_or3_b32 v100, v100, v36, s16
	v_accvgpr_read_b32 v126, a12
	v_lshlrev_b64 v[100:101], 2, v[100:101]
	global_store_dword v[102:103], v104, off sc1
	s_waitcnt lgkmcnt(0)
	v_add_f32_e32 v38, v126, v108
	v_lshl_add_u64 v[102:103], s[14:15], 0, v[100:101]
	v_lshl_add_u64 v[100:101], s[2:3], 0, v[100:101]
	global_store_dword v[100:101], v38, off sc1
	v_or_b32_e32 v100, 25, v0
	v_mov_b32_e32 v101, v1
	v_accvgpr_read_b32 v125, a13
	v_mul_f32_e32 v104, v11, v38
	v_lshl_add_u64 v[100:101], s[0:1], 0, v[100:101]
	v_fmac_f32_e32 v104, v10, v99
	v_lshlrev_b64 v[100:101], 12, v[100:101]
	v_add_f32_e32 v38, v125, v109
	global_store_dword v[102:103], v104, off sc1
	v_or3_b32 v101, v101, 0, 0
	v_or3_b32 v100, v100, v36, s16
	v_mul_f32_e32 v102, v11, v38
	v_fmac_f32_e32 v102, v10, v98
	v_lshlrev_b64 v[98:99], 2, v[100:101]
	v_lshl_add_u64 v[100:101], s[14:15], 0, v[98:99]
	v_lshl_add_u64 v[98:99], s[2:3], 0, v[98:99]
	global_store_dword v[98:99], v38, off sc1
	v_or_b32_e32 v98, 26, v0
	v_mov_b32_e32 v99, v1
	v_lshl_add_u64 v[98:99], s[0:1], 0, v[98:99]
	v_lshlrev_b64 v[98:99], 12, v[98:99]
	v_or3_b32 v99, v99, 0, 0
	v_or3_b32 v98, v98, v36, s16
	v_accvgpr_read_b32 v124, a14
	v_lshlrev_b64 v[98:99], 2, v[98:99]
	global_store_dword v[100:101], v102, off sc1
	v_add_f32_e32 v38, v124, v110
	v_lshl_add_u64 v[100:101], s[14:15], 0, v[98:99]
	v_lshl_add_u64 v[98:99], s[2:3], 0, v[98:99]
	global_store_dword v[98:99], v38, off sc1
	v_or_b32_e32 v98, 27, v0
	v_mov_b32_e32 v99, v1
	v_accvgpr_read_b32 v123, a15
	v_mul_f32_e32 v102, v11, v38
	v_lshl_add_u64 v[98:99], s[0:1], 0, v[98:99]
	v_fmac_f32_e32 v102, v10, v97
	v_lshlrev_b64 v[98:99], 12, v[98:99]
	v_add_f32_e32 v38, v123, v111
	global_store_dword v[100:101], v102, off sc1
	v_or3_b32 v99, v99, 0, 0
	v_or3_b32 v98, v98, v36, s16
	v_mul_f32_e32 v100, v11, v38
	v_fmac_f32_e32 v100, v10, v96
	v_lshlrev_b64 v[96:97], 2, v[98:99]
	v_lshl_add_u64 v[98:99], s[14:15], 0, v[96:97]
	v_lshl_add_u64 v[96:97], s[2:3], 0, v[96:97]
	global_store_dword v[96:97], v38, off sc1
	v_or_b32_e32 v96, 32, v0
	v_mov_b32_e32 v97, v1
	global_store_dword v[98:99], v100, off sc1
	v_lshl_add_u64 v[100:101], s[0:1], 0, v[96:97]
	ds_read_b128 v[96:99], v32 offset:16512
	v_lshlrev_b64 v[100:101], 12, v[100:101]
	v_or3_b32 v105, v101, 0, 0
	v_or3_b32 v104, v100, v36, s16
	v_accvgpr_read_b32 v122, a16
	v_lshlrev_b64 v[104:105], 2, v[104:105]
	ds_read_b128 v[100:103], v32 offset:16544
	s_waitcnt lgkmcnt(1)
	v_add_f32_e32 v38, v122, v96
	v_lshl_add_u64 v[106:107], s[14:15], 0, v[104:105]
	v_lshl_add_u64 v[104:105], s[2:3], 0, v[104:105]
	global_store_dword v[104:105], v38, off sc1
	v_or_b32_e32 v104, 33, v0
	v_mov_b32_e32 v105, v1
	v_accvgpr_read_b32 v121, a17
	v_mul_f32_e32 v96, v11, v38
	v_lshl_add_u64 v[104:105], s[0:1], 0, v[104:105]
	v_fmac_f32_e32 v96, v10, v95
	v_lshlrev_b64 v[104:105], 12, v[104:105]
	v_add_f32_e32 v38, v121, v97
	global_store_dword v[106:107], v96, off sc1
	v_or3_b32 v105, v105, 0, 0
	v_or3_b32 v104, v104, v36, s16
	v_mul_f32_e32 v106, v11, v38
	v_fmac_f32_e32 v106, v10, v94
	v_lshlrev_b64 v[94:95], 2, v[104:105]
	v_lshl_add_u64 v[96:97], s[14:15], 0, v[94:95]
	v_lshl_add_u64 v[94:95], s[2:3], 0, v[94:95]
	global_store_dword v[94:95], v38, off sc1
	v_or_b32_e32 v94, 34, v0
	v_mov_b32_e32 v95, v1
	v_lshl_add_u64 v[94:95], s[0:1], 0, v[94:95]
	v_lshlrev_b64 v[94:95], 12, v[94:95]
	v_or3_b32 v95, v95, 0, 0
	v_or3_b32 v94, v94, v36, s16
	v_accvgpr_read_b32 v120, a18
	v_lshlrev_b64 v[94:95], 2, v[94:95]
	global_store_dword v[96:97], v106, off sc1
	v_add_f32_e32 v38, v120, v98
	v_lshl_add_u64 v[96:97], s[14:15], 0, v[94:95]
	v_lshl_add_u64 v[94:95], s[2:3], 0, v[94:95]
	global_store_dword v[94:95], v38, off sc1
	v_or_b32_e32 v94, 35, v0
	v_mov_b32_e32 v95, v1
	v_accvgpr_read_b32 v119, a19
	v_mul_f32_e32 v98, v11, v38
	v_lshl_add_u64 v[94:95], s[0:1], 0, v[94:95]
	v_fmac_f32_e32 v98, v10, v93
	v_lshlrev_b64 v[94:95], 12, v[94:95]
	v_add_f32_e32 v38, v119, v99
	global_store_dword v[96:97], v98, off sc1
	v_or3_b32 v95, v95, 0, 0
	v_or3_b32 v94, v94, v36, s16
	v_mul_f32_e32 v96, v11, v38
	v_fmac_f32_e32 v96, v10, v92
	v_lshlrev_b64 v[92:93], 2, v[94:95]
	v_lshl_add_u64 v[94:95], s[14:15], 0, v[92:93]
	v_lshl_add_u64 v[92:93], s[2:3], 0, v[92:93]
	global_store_dword v[92:93], v38, off sc1
	v_or_b32_e32 v92, 40, v0
	v_mov_b32_e32 v93, v1
	v_lshl_add_u64 v[92:93], s[0:1], 0, v[92:93]
	v_lshlrev_b64 v[92:93], 12, v[92:93]
	v_or3_b32 v93, v93, 0, 0
	v_or3_b32 v92, v92, v36, s16
	v_accvgpr_read_b32 v118, a20
	v_lshlrev_b64 v[92:93], 2, v[92:93]
	global_store_dword v[94:95], v96, off sc1
	s_waitcnt lgkmcnt(0)
	v_add_f32_e32 v38, v118, v100
	v_lshl_add_u64 v[94:95], s[14:15], 0, v[92:93]
	v_lshl_add_u64 v[92:93], s[2:3], 0, v[92:93]
	global_store_dword v[92:93], v38, off sc1
	v_or_b32_e32 v92, 41, v0
	v_mov_b32_e32 v93, v1
	v_accvgpr_read_b32 v117, a21
	v_mul_f32_e32 v96, v11, v38
	v_lshl_add_u64 v[92:93], s[0:1], 0, v[92:93]
	v_fmac_f32_e32 v96, v10, v91
	v_lshlrev_b64 v[92:93], 12, v[92:93]
	v_add_f32_e32 v38, v117, v101
	global_store_dword v[94:95], v96, off sc1
	v_or3_b32 v93, v93, 0, 0
	v_or3_b32 v92, v92, v36, s16
	v_mul_f32_e32 v94, v11, v38
	v_fmac_f32_e32 v94, v10, v90
	v_lshlrev_b64 v[90:91], 2, v[92:93]
	v_lshl_add_u64 v[92:93], s[14:15], 0, v[90:91]
	v_lshl_add_u64 v[90:91], s[2:3], 0, v[90:91]
	global_store_dword v[90:91], v38, off sc1
	v_or_b32_e32 v90, 42, v0
	v_mov_b32_e32 v91, v1
	v_lshl_add_u64 v[90:91], s[0:1], 0, v[90:91]
	v_lshlrev_b64 v[90:91], 12, v[90:91]
	v_or3_b32 v91, v91, 0, 0
	v_or3_b32 v90, v90, v36, s16
	v_accvgpr_read_b32 v116, a22
	v_lshlrev_b64 v[90:91], 2, v[90:91]
	global_store_dword v[92:93], v94, off sc1
	v_add_f32_e32 v38, v116, v102
	v_lshl_add_u64 v[92:93], s[14:15], 0, v[90:91]
	v_lshl_add_u64 v[90:91], s[2:3], 0, v[90:91]
	global_store_dword v[90:91], v38, off sc1
	v_or_b32_e32 v90, 43, v0
	v_mov_b32_e32 v91, v1
	v_accvgpr_read_b32 v115, a23
	v_mul_f32_e32 v94, v11, v38
	v_lshl_add_u64 v[90:91], s[0:1], 0, v[90:91]
	v_fmac_f32_e32 v94, v10, v89
	v_lshlrev_b64 v[90:91], 12, v[90:91]
	v_add_f32_e32 v38, v115, v103
	global_store_dword v[92:93], v94, off sc1
	v_or3_b32 v91, v91, 0, 0
	v_or3_b32 v90, v90, v36, s16
	v_mul_f32_e32 v92, v11, v38
	v_fmac_f32_e32 v92, v10, v88
	v_lshlrev_b64 v[88:89], 2, v[90:91]
	v_lshl_add_u64 v[90:91], s[14:15], 0, v[88:89]
	v_lshl_add_u64 v[88:89], s[2:3], 0, v[88:89]
	global_store_dword v[88:89], v38, off sc1
	v_or_b32_e32 v88, 48, v0
	v_mov_b32_e32 v89, v1
	global_store_dword v[90:91], v92, off sc1
	v_lshl_add_u64 v[92:93], s[0:1], 0, v[88:89]
	ds_read_b128 v[88:91], v32 offset:16576
	v_lshlrev_b64 v[92:93], 12, v[92:93]
	v_or3_b32 v97, v93, 0, 0
	v_or3_b32 v96, v92, v36, s16
	v_accvgpr_read_b32 v114, a24
	v_lshlrev_b64 v[96:97], 2, v[96:97]
	ds_read_b128 v[92:95], v32 offset:16608
	s_waitcnt lgkmcnt(1)
	v_add_f32_e32 v38, v114, v88
	v_lshl_add_u64 v[98:99], s[14:15], 0, v[96:97]
	v_lshl_add_u64 v[96:97], s[2:3], 0, v[96:97]
	global_store_dword v[96:97], v38, off sc1
	v_or_b32_e32 v96, 49, v0
	v_mov_b32_e32 v97, v1
	v_accvgpr_read_b32 v113, a25
	v_mul_f32_e32 v88, v11, v38
	v_lshl_add_u64 v[96:97], s[0:1], 0, v[96:97]
	v_fmac_f32_e32 v88, v10, v87
	v_lshlrev_b64 v[96:97], 12, v[96:97]
	v_add_f32_e32 v38, v113, v89
	global_store_dword v[98:99], v88, off sc1
	v_or3_b32 v97, v97, 0, 0
	v_or3_b32 v96, v96, v36, s16
	v_mul_f32_e32 v98, v11, v38
	v_fmac_f32_e32 v98, v10, v86
	v_lshlrev_b64 v[86:87], 2, v[96:97]
	v_lshl_add_u64 v[88:89], s[14:15], 0, v[86:87]
	v_lshl_add_u64 v[86:87], s[2:3], 0, v[86:87]
	global_store_dword v[86:87], v38, off sc1
	v_or_b32_e32 v86, 50, v0
	v_mov_b32_e32 v87, v1
	v_lshl_add_u64 v[86:87], s[0:1], 0, v[86:87]
	v_lshlrev_b64 v[86:87], 12, v[86:87]
	v_or3_b32 v87, v87, 0, 0
	v_or3_b32 v86, v86, v36, s16
	v_accvgpr_read_b32 v47, a26
	v_lshlrev_b64 v[86:87], 2, v[86:87]
	global_store_dword v[88:89], v98, off sc1
	v_add_f32_e32 v38, v47, v90
	v_lshl_add_u64 v[88:89], s[14:15], 0, v[86:87]
	v_lshl_add_u64 v[86:87], s[2:3], 0, v[86:87]
	global_store_dword v[86:87], v38, off sc1
	v_or_b32_e32 v86, 51, v0
	v_mov_b32_e32 v87, v1
	v_lshl_add_u64 v[86:87], s[0:1], 0, v[86:87]
	v_accvgpr_read_b32 v46, a27
	v_mul_f32_e32 v47, v11, v38
	v_lshlrev_b64 v[86:87], 12, v[86:87]
	v_fmac_f32_e32 v47, v10, v85
	v_or3_b32 v87, v87, 0, 0
	v_or3_b32 v86, v86, v36, s16
	v_add_f32_e32 v38, v46, v91
	global_store_dword v[88:89], v47, off sc1
	v_mul_f32_e32 v88, v11, v38
	v_lshlrev_b64 v[46:47], 2, v[86:87]
	v_fmac_f32_e32 v88, v10, v84
	v_lshl_add_u64 v[84:85], s[14:15], 0, v[46:47]
	v_lshl_add_u64 v[46:47], s[2:3], 0, v[46:47]
	global_store_dword v[46:47], v38, off sc1
	v_or_b32_e32 v46, 56, v0
	v_mov_b32_e32 v47, v1
	v_lshl_add_u64 v[46:47], s[0:1], 0, v[46:47]
	v_lshlrev_b64 v[46:47], 12, v[46:47]
	v_or3_b32 v47, v47, 0, 0
	v_or3_b32 v46, v46, v36, s16
	v_accvgpr_read_b32 v44, a28
	v_lshlrev_b64 v[46:47], 2, v[46:47]
	global_store_dword v[84:85], v88, off sc1
	s_waitcnt lgkmcnt(0)
	v_add_f32_e32 v38, v44, v92
	v_lshl_add_u64 v[84:85], s[14:15], 0, v[46:47]
	v_lshl_add_u64 v[46:47], s[2:3], 0, v[46:47]
	global_store_dword v[46:47], v38, off sc1
	v_or_b32_e32 v46, 57, v0
	v_mov_b32_e32 v47, v1
	v_lshl_add_u64 v[46:47], s[0:1], 0, v[46:47]
	v_accvgpr_read_b32 v42, a29
	v_lshlrev_b64 v[46:47], 12, v[46:47]
	v_mul_f32_e32 v44, v11, v38
	v_or3_b32 v47, v47, 0, 0
	v_or3_b32 v46, v46, v36, s16
	v_add_f32_e32 v38, v42, v93
	v_mul_f32_e32 v42, v11, v38
	v_lshlrev_b64 v[46:47], 2, v[46:47]
	v_fmac_f32_e32 v44, v10, v83
	v_fmac_f32_e32 v42, v10, v82
	v_lshl_add_u64 v[82:83], s[14:15], 0, v[46:47]
	v_lshl_add_u64 v[46:47], s[2:3], 0, v[46:47]
	global_store_dword v[84:85], v44, off sc1
	global_store_dword v[46:47], v38, off sc1
	v_or_b32_e32 v46, 58, v0
	v_mov_b32_e32 v47, v1
	v_lshl_add_u64 v[46:47], s[0:1], 0, v[46:47]
	v_lshlrev_b64 v[46:47], 12, v[46:47]
	v_or3_b32 v47, v47, 0, 0
	v_or3_b32 v46, v46, v36, s16
	v_accvgpr_read_b32 v41, a30
	v_lshlrev_b64 v[46:47], 2, v[46:47]
	global_store_dword v[82:83], v42, off sc1
	v_add_f32_e32 v38, v41, v94
	v_lshl_add_u64 v[82:83], s[14:15], 0, v[46:47]
	v_lshl_add_u64 v[46:47], s[2:3], 0, v[46:47]
	global_store_dword v[46:47], v38, off sc1
	v_or_b32_e32 v46, 59, v0
	v_mov_b32_e32 v47, v1
	v_lshl_add_u64 v[46:47], s[0:1], 0, v[46:47]
	v_mul_f32_e32 v41, v11, v38
	v_lshlrev_b64 v[46:47], 12, v[46:47]
	v_accvgpr_read_b32 v40, a31
	v_fmac_f32_e32 v41, v10, v81
	v_or3_b32 v47, v47, 0, 0
	v_or3_b32 v46, v46, v36, s16
	global_store_dword v[82:83], v41, off sc1
	v_add_f32_e32 v38, v40, v95
	v_lshlrev_b64 v[40:41], 2, v[46:47]
	v_lshl_add_u64 v[46:47], s[14:15], 0, v[40:41]
	v_lshl_add_u64 v[40:41], s[2:3], 0, v[40:41]
	ds_read_b128 v[82:85], v32 offset:16640
	ds_read_b128 v[86:89], v32 offset:16672
	global_store_dword v[40:41], v38, off sc1
	v_or_b32_e32 v40, 64, v0
	v_mov_b32_e32 v41, v1
	v_lshl_add_u64 v[40:41], s[0:1], 0, v[40:41]
	v_mul_f32_e32 v42, v11, v38
	v_lshlrev_b64 v[40:41], 12, v[40:41]
	v_accvgpr_read_b32 v39, a32
	v_fmac_f32_e32 v42, v10, v79
	v_or3_b32 v41, v41, 0, 0
	v_or3_b32 v40, v40, v36, s16
	global_store_dword v[46:47], v42, off sc1
	s_waitcnt lgkmcnt(1)
	v_add_f32_e32 v42, v39, v82
	v_lshlrev_b64 v[38:39], 2, v[40:41]
	v_lshl_add_u64 v[40:41], s[14:15], 0, v[38:39]
	v_lshl_add_u64 v[38:39], s[2:3], 0, v[38:39]
	global_store_dword v[38:39], v42, off sc1
	v_or_b32_e32 v38, 0x41, v0
	v_mov_b32_e32 v39, v1
	v_lshl_add_u64 v[38:39], s[0:1], 0, v[38:39]
	v_lshlrev_b64 v[38:39], 12, v[38:39]
	v_mul_f32_e32 v44, v11, v42
	v_or3_b32 v39, v39, 0, 0
	v_or3_b32 v38, v38, v36, s16
	v_accvgpr_read_b32 v35, a33
	v_fmac_f32_e32 v44, v10, v71
	v_lshlrev_b64 v[38:39], 2, v[38:39]
	global_store_dword v[40:41], v44, off sc1
	v_add_f32_e32 v35, v35, v83
	v_lshl_add_u64 v[40:41], s[14:15], 0, v[38:39]
	v_lshl_add_u64 v[38:39], s[2:3], 0, v[38:39]
	global_store_dword v[38:39], v35, off sc1
	v_or_b32_e32 v38, 0x42, v0
	v_mov_b32_e32 v39, v1
	v_lshl_add_u64 v[38:39], s[0:1], 0, v[38:39]
	v_mul_f32_e32 v42, v11, v35
	v_lshlrev_b64 v[38:39], 12, v[38:39]
	v_accvgpr_read_b32 v34, a34
	v_fmac_f32_e32 v42, v10, v68
	v_or3_b32 v39, v39, 0, 0
	v_or3_b32 v38, v38, v36, s16
	global_store_dword v[40:41], v42, off sc1
	v_add_f32_e32 v40, v34, v84
	v_lshlrev_b64 v[34:35], 2, v[38:39]
	v_lshl_add_u64 v[38:39], s[14:15], 0, v[34:35]
	v_lshl_add_u64 v[34:35], s[2:3], 0, v[34:35]
	global_store_dword v[34:35], v40, off sc1
	v_or_b32_e32 v34, 0x43, v0
	v_mov_b32_e32 v35, v1
	v_lshl_add_u64 v[34:35], s[0:1], 0, v[34:35]
	v_lshlrev_b64 v[34:35], 12, v[34:35]
	v_mul_f32_e32 v41, v11, v40
	v_or3_b32 v35, v35, 0, 0
	v_or3_b32 v34, v34, v36, s16
	v_accvgpr_read_b32 v33, a35
	v_fmac_f32_e32 v41, v10, v65
	v_lshlrev_b64 v[34:35], 2, v[34:35]
	global_store_dword v[38:39], v41, off sc1
	v_add_f32_e32 v33, v33, v85
	v_lshl_add_u64 v[38:39], s[14:15], 0, v[34:35]
	v_lshl_add_u64 v[34:35], s[2:3], 0, v[34:35]
	global_store_dword v[34:35], v33, off sc1
	v_or_b32_e32 v34, 0x48, v0
	v_mov_b32_e32 v35, v1
	v_lshl_add_u64 v[34:35], s[0:1], 0, v[34:35]
	v_lshlrev_b64 v[34:35], 12, v[34:35]
	v_mul_f32_e32 v40, v11, v33
	v_or3_b32 v35, v35, 0, 0
	v_or3_b32 v34, v34, v36, s16
	v_accvgpr_read_b32 v31, a36
	v_fmac_f32_e32 v40, v10, v63
	v_lshlrev_b64 v[34:35], 2, v[34:35]
	global_store_dword v[38:39], v40, off sc1
	s_waitcnt lgkmcnt(0)
	v_add_f32_e32 v31, v31, v86
	v_lshl_add_u64 v[38:39], s[14:15], 0, v[34:35]
	v_lshl_add_u64 v[34:35], s[2:3], 0, v[34:35]
	global_store_dword v[34:35], v31, off sc1
	v_or_b32_e32 v34, 0x49, v0
	v_mov_b32_e32 v35, v1
	v_lshl_add_u64 v[34:35], s[0:1], 0, v[34:35]
	v_mul_f32_e32 v33, v11, v31
	v_lshlrev_b64 v[34:35], 12, v[34:35]
	v_accvgpr_read_b32 v30, a37
	v_fmac_f32_e32 v33, v10, v61
	v_or3_b32 v35, v35, 0, 0
	v_or3_b32 v34, v34, v36, s16
	global_store_dword v[38:39], v33, off sc1
	v_add_f32_e32 v33, v30, v87
	v_lshlrev_b64 v[30:31], 2, v[34:35]
	v_lshl_add_u64 v[34:35], s[14:15], 0, v[30:31]
	v_lshl_add_u64 v[30:31], s[2:3], 0, v[30:31]
	global_store_dword v[30:31], v33, off sc1
	v_or_b32_e32 v30, 0x4a, v0
	v_mov_b32_e32 v31, v1
	v_lshl_add_u64 v[30:31], s[0:1], 0, v[30:31]
	v_lshlrev_b64 v[30:31], 12, v[30:31]
	v_mul_f32_e32 v38, v11, v33
	v_or3_b32 v31, v31, 0, 0
	v_or3_b32 v30, v30, v36, s16
	v_accvgpr_read_b32 v29, a38
	v_fmac_f32_e32 v38, v10, v60
	v_lshlrev_b64 v[30:31], 2, v[30:31]
	global_store_dword v[34:35], v38, off sc1
	v_add_f32_e32 v29, v29, v88
	v_lshl_add_u64 v[34:35], s[14:15], 0, v[30:31]
	v_lshl_add_u64 v[30:31], s[2:3], 0, v[30:31]
	global_store_dword v[30:31], v29, off sc1
	v_or_b32_e32 v30, 0x4b, v0
	v_mov_b32_e32 v31, v1
	v_lshl_add_u64 v[30:31], s[0:1], 0, v[30:31]
	v_mul_f32_e32 v33, v11, v29
	v_lshlrev_b64 v[30:31], 12, v[30:31]
	v_accvgpr_read_b32 v28, a39
	v_fmac_f32_e32 v33, v10, v59
	v_or3_b32 v31, v31, 0, 0
	v_or3_b32 v30, v30, v36, s16
	global_store_dword v[34:35], v33, off sc1
	v_add_f32_e32 v33, v28, v89
	v_lshlrev_b64 v[28:29], 2, v[30:31]
	v_mul_f32_e32 v34, v11, v33
	v_lshl_add_u64 v[30:31], s[14:15], 0, v[28:29]
	v_lshl_add_u64 v[28:29], s[2:3], 0, v[28:29]
	v_fmac_f32_e32 v34, v10, v58
	global_store_dword v[28:29], v33, off sc1
	v_or_b32_e32 v28, 0x50, v0
	v_mov_b32_e32 v29, v1
	global_store_dword v[30:31], v34, off sc1
	v_lshl_add_u64 v[34:35], s[0:1], 0, v[28:29]
	ds_read_b128 v[28:31], v32 offset:16704
	v_lshlrev_b64 v[34:35], 12, v[34:35]
	v_or3_b32 v39, v35, 0, 0
	v_or3_b32 v38, v34, v36, s16
	v_accvgpr_read_b32 v27, a40
	v_lshlrev_b64 v[38:39], 2, v[38:39]
	s_waitcnt lgkmcnt(0)
	v_add_f32_e32 v27, v27, v28
	v_lshl_add_u64 v[40:41], s[14:15], 0, v[38:39]
	v_lshl_add_u64 v[38:39], s[2:3], 0, v[38:39]
	global_store_dword v[38:39], v27, off sc1
	v_or_b32_e32 v38, 0x51, v0
	v_mov_b32_e32 v39, v1
	v_lshl_add_u64 v[38:39], s[0:1], 0, v[38:39]
	v_mul_f32_e32 v28, v11, v27
	v_lshlrev_b64 v[38:39], 12, v[38:39]
	v_accvgpr_read_b32 v26, a41
	v_fmac_f32_e32 v28, v10, v57
	v_or3_b32 v39, v39, 0, 0
	v_or3_b32 v38, v38, v36, s16
	global_store_dword v[40:41], v28, off sc1
	v_add_f32_e32 v40, v26, v29
	v_lshlrev_b64 v[26:27], 2, v[38:39]
	v_lshl_add_u64 v[28:29], s[14:15], 0, v[26:27]
	v_lshl_add_u64 v[26:27], s[2:3], 0, v[26:27]
	global_store_dword v[26:27], v40, off sc1
	v_or_b32_e32 v26, 0x52, v0
	v_mov_b32_e32 v27, v1
	v_lshl_add_u64 v[26:27], s[0:1], 0, v[26:27]
	v_lshlrev_b64 v[26:27], 12, v[26:27]
	v_mul_f32_e32 v41, v11, v40
	v_or3_b32 v27, v27, 0, 0
	v_or3_b32 v26, v26, v36, s16
	v_accvgpr_read_b32 v25, a42
	v_fmac_f32_e32 v41, v10, v56
	v_lshlrev_b64 v[26:27], 2, v[26:27]
	global_store_dword v[28:29], v41, off sc1
	v_add_f32_e32 v25, v25, v30
	v_lshl_add_u64 v[28:29], s[14:15], 0, v[26:27]
	v_lshl_add_u64 v[26:27], s[2:3], 0, v[26:27]
	global_store_dword v[26:27], v25, off sc1
	v_or_b32_e32 v26, 0x53, v0
	v_mov_b32_e32 v27, v1
	v_lshl_add_u64 v[26:27], s[0:1], 0, v[26:27]
	v_mul_f32_e32 v30, v11, v25
	v_lshlrev_b64 v[26:27], 12, v[26:27]
	v_accvgpr_read_b32 v24, a43
	v_fmac_f32_e32 v30, v10, v55
	v_or3_b32 v27, v27, 0, 0
	v_or3_b32 v26, v26, v36, s16
	global_store_dword v[28:29], v30, off sc1
	v_add_f32_e32 v28, v24, v31
	v_lshlrev_b64 v[24:25], 2, v[26:27]
	v_lshl_add_u64 v[26:27], s[14:15], 0, v[24:25]
	v_lshl_add_u64 v[24:25], s[2:3], 0, v[24:25]
	ds_read_b128 v[32:35], v32 offset:16736
	global_store_dword v[24:25], v28, off sc1
	v_or_b32_e32 v24, 0x58, v0
	v_mov_b32_e32 v25, v1
	v_lshl_add_u64 v[24:25], s[0:1], 0, v[24:25]
	v_lshlrev_b64 v[24:25], 12, v[24:25]
	v_mul_f32_e32 v29, v11, v28
	v_or3_b32 v25, v25, 0, 0
	v_or3_b32 v24, v24, v36, s16
	v_accvgpr_read_b32 v23, a44
	v_fmac_f32_e32 v29, v10, v54
	v_lshlrev_b64 v[24:25], 2, v[24:25]
	global_store_dword v[26:27], v29, off sc1
	s_waitcnt lgkmcnt(0)
	v_add_f32_e32 v23, v23, v32
	v_lshl_add_u64 v[26:27], s[14:15], 0, v[24:25]
	v_lshl_add_u64 v[24:25], s[2:3], 0, v[24:25]
	global_store_dword v[24:25], v23, off sc1
	v_or_b32_e32 v24, 0x59, v0
	v_mov_b32_e32 v25, v1
	v_lshl_add_u64 v[24:25], s[0:1], 0, v[24:25]
	v_mul_f32_e32 v28, v11, v23
	v_lshlrev_b64 v[24:25], 12, v[24:25]
	v_accvgpr_read_b32 v22, a45
	v_fmac_f32_e32 v28, v10, v53
	v_or3_b32 v25, v25, 0, 0
	v_or3_b32 v24, v24, v36, s16
	global_store_dword v[26:27], v28, off sc1
	v_add_f32_e32 v26, v22, v33
	v_lshlrev_b64 v[22:23], 2, v[24:25]
	v_lshl_add_u64 v[24:25], s[14:15], 0, v[22:23]
	v_lshl_add_u64 v[22:23], s[2:3], 0, v[22:23]
	global_store_dword v[22:23], v26, off sc1
	v_or_b32_e32 v22, 0x5a, v0
	v_mov_b32_e32 v23, v1
	v_lshl_add_u64 v[22:23], s[0:1], 0, v[22:23]
	v_lshlrev_b64 v[22:23], 12, v[22:23]
	v_mul_f32_e32 v27, v11, v26
	v_or3_b32 v23, v23, 0, 0
	v_or3_b32 v22, v22, v36, s16
	v_accvgpr_read_b32 v21, a46
	v_fmac_f32_e32 v27, v10, v52
	v_lshlrev_b64 v[22:23], 2, v[22:23]
	global_store_dword v[24:25], v27, off sc1
	v_add_f32_e32 v21, v21, v34
	v_lshl_add_u64 v[24:25], s[14:15], 0, v[22:23]
	v_lshl_add_u64 v[22:23], s[2:3], 0, v[22:23]
	v_or_b32_e32 v0, 0x5b, v0
	global_store_dword v[22:23], v21, off sc1
	v_lshl_add_u64 v[22:23], s[0:1], 0, v[0:1]
	v_lshlrev_b64 v[22:23], 12, v[22:23]
	v_accvgpr_read_b32 v20, a47
	v_or3_b32 v23, v23, 0, 0
	v_or3_b32 v22, v22, v36, s16
	v_mul_f32_e32 v26, v11, v21
	v_add_f32_e32 v0, v20, v35
	v_lshlrev_b64 v[20:21], 2, v[22:23]
	v_lshlrev_b32_e32 v38, 5, v48
	v_fmac_f32_e32 v26, v10, v51
	v_lshl_add_u64 v[22:23], s[14:15], 0, v[20:21]
	v_lshl_add_u64 v[20:21], s[2:3], 0, v[20:21]
	v_or_b32_e32 v39, v38, v49
	global_store_dword v[24:25], v26, off sc1
	v_mul_f32_e32 v24, v11, v0
	global_store_dword v[20:21], v0, off sc1
	v_or_b32_e32 v0, 0x60, v39
	v_fmac_f32_e32 v24, v10, v50
	v_lshl_add_u64 v[20:21], s[0:1], 0, v[0:1]
	v_lshlrev_b32_e32 v34, 2, v0
	v_or_b32_e32 v0, 0x61, v39
	global_store_dword v[22:23], v24, off sc1
	v_lshl_add_u64 v[22:23], s[0:1], 0, v[0:1]
	v_lshlrev_b32_e32 v35, 2, v0
	v_or_b32_e32 v0, 0x62, v39
	v_lshl_add_u64 v[24:25], s[0:1], 0, v[0:1]
	v_lshlrev_b32_e32 v40, 2, v0
	v_or_b32_e32 v0, 0x63, v39
	v_lshl_add_u64 v[26:27], s[0:1], 0, v[0:1]
	v_lshlrev_b32_e32 v41, 2, v0
	v_or_b32_e32 v0, 0x68, v39
	v_lshl_add_u64 v[28:29], s[0:1], 0, v[0:1]
	v_lshlrev_b32_e32 v42, 2, v0
	v_or_b32_e32 v0, 0x69, v39
	v_lshl_add_u64 v[30:31], s[0:1], 0, v[0:1]
	v_lshlrev_b32_e32 v44, 2, v0
	v_or_b32_e32 v0, 0x6a, v39
	v_lshlrev_b64 v[20:21], 12, v[20:21]
	v_lshl_add_u64 v[32:33], s[0:1], 0, v[0:1]
	v_lshlrev_b32_e32 v46, 2, v0
	v_or_b32_e32 v0, 0x6b, v39
	v_or3_b32 v21, v21, 0, 0
	v_or3_b32 v20, v20, v36, s16
	v_lshlrev_b32_e32 v47, 2, v0
	v_accvgpr_read_b32 v19, a48
	ds_read_b32 v34, v34 offset:16384
	ds_read_b32 v48, v35 offset:16384
	ds_read_b32 v40, v40 offset:16384
	ds_read_b32 v41, v41 offset:16384
	ds_read_b32 v42, v42 offset:16384
	ds_read_b32 v44, v44 offset:16384
	ds_read_b32 v46, v46 offset:16384
	ds_read_b32 v47, v47 offset:16384
	v_lshlrev_b64 v[20:21], 2, v[20:21]
	s_waitcnt lgkmcnt(7)
	v_add_f32_e32 v19, v19, v34
	v_lshl_add_u64 v[34:35], s[14:15], 0, v[20:21]
	v_lshl_add_u64 v[20:21], s[2:3], 0, v[20:21]
	global_store_dword v[20:21], v19, off sc1
	v_lshlrev_b64 v[20:21], 12, v[22:23]
	v_accvgpr_read_b32 v18, a49
	v_or3_b32 v21, v21, 0, 0
	v_or3_b32 v20, v20, v36, s16
	v_mul_f32_e32 v49, v11, v19
	s_waitcnt lgkmcnt(6)
	v_add_f32_e32 v22, v18, v48
	v_lshlrev_b64 v[18:19], 2, v[20:21]
	v_fmac_f32_e32 v49, v10, v80
	v_lshl_add_u64 v[20:21], s[14:15], 0, v[18:19]
	v_lshl_add_u64 v[18:19], s[2:3], 0, v[18:19]
	global_store_dword v[34:35], v49, off sc1
	global_store_dword v[18:19], v22, off sc1
	v_lshlrev_b64 v[18:19], 12, v[24:25]
	v_mul_f32_e32 v23, v11, v22
	v_or3_b32 v19, v19, 0, 0
	v_or3_b32 v18, v18, v36, s16
	v_accvgpr_read_b32 v17, a50
	v_fmac_f32_e32 v23, v10, v78
	v_lshlrev_b64 v[18:19], 2, v[18:19]
	global_store_dword v[20:21], v23, off sc1
	s_waitcnt lgkmcnt(5)
	v_add_f32_e32 v17, v17, v40
	v_lshl_add_u64 v[20:21], s[14:15], 0, v[18:19]
	v_lshl_add_u64 v[18:19], s[2:3], 0, v[18:19]
	v_mul_f32_e32 v22, v11, v17
	global_store_dword v[18:19], v17, off sc1
	v_lshlrev_b64 v[18:19], 12, v[26:27]
	v_accvgpr_read_b32 v16, a51
	v_fmac_f32_e32 v22, v10, v77
	v_or3_b32 v19, v19, 0, 0
	v_or3_b32 v18, v18, v36, s16
	global_store_dword v[20:21], v22, off sc1
	s_waitcnt lgkmcnt(4)
	v_add_f32_e32 v20, v16, v41
	v_lshlrev_b64 v[16:17], 2, v[18:19]
	v_lshl_add_u64 v[18:19], s[14:15], 0, v[16:17]
	v_lshl_add_u64 v[16:17], s[2:3], 0, v[16:17]
	global_store_dword v[16:17], v20, off sc1
	v_lshlrev_b64 v[16:17], 12, v[28:29]
	v_mul_f32_e32 v21, v11, v20
	v_or3_b32 v17, v17, 0, 0
	v_or3_b32 v16, v16, v36, s16
	v_accvgpr_read_b32 v15, a52
	v_fmac_f32_e32 v21, v10, v76
	v_lshlrev_b64 v[16:17], 2, v[16:17]
	global_store_dword v[18:19], v21, off sc1
	s_waitcnt lgkmcnt(3)
	v_add_f32_e32 v15, v15, v42
	v_lshl_add_u64 v[18:19], s[14:15], 0, v[16:17]
	v_lshl_add_u64 v[16:17], s[2:3], 0, v[16:17]
	v_mul_f32_e32 v20, v11, v15
	global_store_dword v[16:17], v15, off sc1
	v_lshlrev_b64 v[16:17], 12, v[30:31]
	v_accvgpr_read_b32 v14, a53
	v_fmac_f32_e32 v20, v10, v75
	v_or3_b32 v17, v17, 0, 0
	v_or3_b32 v16, v16, v36, s16
	global_store_dword v[18:19], v20, off sc1
	s_waitcnt lgkmcnt(2)
	v_add_f32_e32 v18, v14, v44
	v_lshlrev_b64 v[14:15], 2, v[16:17]
	v_lshl_add_u64 v[16:17], s[14:15], 0, v[14:15]
	v_lshl_add_u64 v[14:15], s[2:3], 0, v[14:15]
	global_store_dword v[14:15], v18, off sc1
	v_lshlrev_b64 v[14:15], 12, v[32:33]
	v_mul_f32_e32 v19, v11, v18
	v_or3_b32 v15, v15, 0, 0
	v_or3_b32 v14, v14, v36, s16
	v_accvgpr_read_b32 v13, a54
	v_fmac_f32_e32 v19, v10, v74
	v_lshlrev_b64 v[14:15], 2, v[14:15]
	global_store_dword v[16:17], v19, off sc1
	s_waitcnt lgkmcnt(1)
	v_add_f32_e32 v13, v13, v46
	v_lshl_add_u64 v[16:17], s[14:15], 0, v[14:15]
	v_lshl_add_u64 v[14:15], s[2:3], 0, v[14:15]
	global_store_dword v[14:15], v13, off sc1
	v_lshl_add_u64 v[14:15], s[0:1], 0, v[0:1]
	v_lshlrev_b64 v[14:15], 12, v[14:15]
	v_accvgpr_read_b32 v12, a55
	v_or3_b32 v15, v15, 0, 0
	v_or3_b32 v14, v14, v36, s16
	v_mul_f32_e32 v18, v11, v13
	s_waitcnt lgkmcnt(0)
	v_add_f32_e32 v0, v12, v47
	v_lshlrev_b64 v[12:13], 2, v[14:15]
	v_fmac_f32_e32 v18, v10, v72
	v_lshl_add_u64 v[14:15], s[14:15], 0, v[12:13]
	v_lshl_add_u64 v[12:13], s[2:3], 0, v[12:13]
	global_store_dword v[16:17], v18, off sc1
	v_mul_f32_e32 v16, v11, v0
	global_store_dword v[12:13], v0, off sc1
	v_or_b32_e32 v0, 0x70, v39
	v_fmac_f32_e32 v16, v10, v69
	v_lshl_add_u64 v[12:13], s[0:1], 0, v[0:1]
	v_lshlrev_b32_e32 v26, 2, v0
	v_or_b32_e32 v0, 0x71, v39
	global_store_dword v[14:15], v16, off sc1
	v_lshl_add_u64 v[14:15], s[0:1], 0, v[0:1]
	v_lshlrev_b32_e32 v27, 2, v0
	v_or_b32_e32 v0, 0x72, v39
	v_lshl_add_u64 v[16:17], s[0:1], 0, v[0:1]
	v_lshlrev_b32_e32 v28, 2, v0
	v_or_b32_e32 v0, 0x73, v39
	v_lshl_add_u64 v[18:19], s[0:1], 0, v[0:1]
	v_lshlrev_b32_e32 v29, 2, v0
	v_or_b32_e32 v0, 0x78, v39
	v_lshl_add_u64 v[20:21], s[0:1], 0, v[0:1]
	v_lshlrev_b32_e32 v30, 2, v0
	v_or_b32_e32 v0, 0x79, v39
	v_lshl_add_u64 v[22:23], s[0:1], 0, v[0:1]
	v_lshlrev_b32_e32 v31, 2, v0
	v_or_b32_e32 v0, 0x7a, v39
	s_movk_i32 s4, 0x7b
	v_lshlrev_b64 v[12:13], 12, v[12:13]
	v_lshl_add_u64 v[24:25], s[0:1], 0, v[0:1]
	v_lshlrev_b32_e32 v32, 2, v0
	v_or3_b32 v0, v38, v37, s4
	v_or3_b32 v13, v13, 0, 0
	v_or3_b32 v12, v12, v36, s16
	v_lshlrev_b32_e32 v33, 2, v0
	v_accvgpr_read_b32 v9, a56
	ds_read_b32 v26, v26 offset:16384
	ds_read_b32 v34, v27 offset:16384
	ds_read_b32 v28, v28 offset:16384
	ds_read_b32 v29, v29 offset:16384
	ds_read_b32 v30, v30 offset:16384
	ds_read_b32 v31, v31 offset:16384
	ds_read_b32 v32, v32 offset:16384
	ds_read_b32 v33, v33 offset:16384
	v_lshlrev_b64 v[12:13], 2, v[12:13]
	s_waitcnt lgkmcnt(7)
	v_add_f32_e32 v9, v9, v26
	v_lshl_add_u64 v[26:27], s[14:15], 0, v[12:13]
	v_lshl_add_u64 v[12:13], s[2:3], 0, v[12:13]
	global_store_dword v[12:13], v9, off sc1
	v_lshlrev_b64 v[12:13], 12, v[14:15]
	v_accvgpr_read_b32 v8, a57
	v_or3_b32 v13, v13, 0, 0
	v_or3_b32 v12, v12, v36, s16
	v_mul_f32_e32 v35, v11, v9
	s_waitcnt lgkmcnt(6)
	v_add_f32_e32 v14, v8, v34
	v_lshlrev_b64 v[8:9], 2, v[12:13]
	v_fmac_f32_e32 v35, v10, v73
	v_lshl_add_u64 v[12:13], s[14:15], 0, v[8:9]
	v_lshl_add_u64 v[8:9], s[2:3], 0, v[8:9]
	global_store_dword v[26:27], v35, off sc1
	global_store_dword v[8:9], v14, off sc1
	v_lshlrev_b64 v[8:9], 12, v[16:17]
	v_mul_f32_e32 v15, v11, v14
	v_or3_b32 v9, v9, 0, 0
	v_or3_b32 v8, v8, v36, s16
	v_accvgpr_read_b32 v7, a58
	v_fmac_f32_e32 v15, v10, v70
	v_lshlrev_b64 v[8:9], 2, v[8:9]
	global_store_dword v[12:13], v15, off sc1
	s_waitcnt lgkmcnt(5)
	v_add_f32_e32 v7, v7, v28
	v_lshl_add_u64 v[12:13], s[14:15], 0, v[8:9]
	v_lshl_add_u64 v[8:9], s[2:3], 0, v[8:9]
	v_mul_f32_e32 v14, v11, v7
	global_store_dword v[8:9], v7, off sc1
	v_lshlrev_b64 v[8:9], 12, v[18:19]
	v_accvgpr_read_b32 v6, a59
	v_fmac_f32_e32 v14, v10, v67
	v_or3_b32 v9, v9, 0, 0
	v_or3_b32 v8, v8, v36, s16
	global_store_dword v[12:13], v14, off sc1
	s_waitcnt lgkmcnt(4)
	v_add_f32_e32 v12, v6, v29
	v_lshlrev_b64 v[6:7], 2, v[8:9]
	v_lshl_add_u64 v[8:9], s[14:15], 0, v[6:7]
	v_lshl_add_u64 v[6:7], s[2:3], 0, v[6:7]
	global_store_dword v[6:7], v12, off sc1
	v_lshlrev_b64 v[6:7], 12, v[20:21]
	v_mul_f32_e32 v13, v11, v12
	v_or3_b32 v7, v7, 0, 0
	v_or3_b32 v6, v6, v36, s16
	v_accvgpr_read_b32 v5, a60
	v_fmac_f32_e32 v13, v10, v66
	v_lshlrev_b64 v[6:7], 2, v[6:7]
	global_store_dword v[8:9], v13, off sc1
	s_waitcnt lgkmcnt(3)
	v_add_f32_e32 v5, v5, v30
	v_lshl_add_u64 v[8:9], s[14:15], 0, v[6:7]
	v_lshl_add_u64 v[6:7], s[2:3], 0, v[6:7]
	v_mul_f32_e32 v12, v11, v5
	global_store_dword v[6:7], v5, off sc1
	v_lshlrev_b64 v[6:7], 12, v[22:23]
	v_accvgpr_read_b32 v4, a61
	v_fmac_f32_e32 v12, v10, v64
	v_or3_b32 v7, v7, 0, 0
	v_or3_b32 v6, v6, v36, s16
	global_store_dword v[8:9], v12, off sc1
	s_waitcnt lgkmcnt(2)
	v_add_f32_e32 v8, v4, v31
	v_lshlrev_b64 v[4:5], 2, v[6:7]
	v_lshl_add_u64 v[6:7], s[14:15], 0, v[4:5]
	v_lshl_add_u64 v[4:5], s[2:3], 0, v[4:5]
	global_store_dword v[4:5], v8, off sc1
	v_lshlrev_b64 v[4:5], 12, v[24:25]
	v_mul_f32_e32 v9, v11, v8
	v_or3_b32 v5, v5, 0, 0
	v_or3_b32 v4, v4, v36, s16
	v_accvgpr_read_b32 v3, a62
	v_fmac_f32_e32 v9, v10, v62
	v_lshlrev_b64 v[4:5], 2, v[4:5]
	v_lshl_add_u64 v[0:1], s[0:1], 0, v[0:1]
	v_accvgpr_read_b32 v2, a63
	global_store_dword v[6:7], v9, off sc1
	s_waitcnt lgkmcnt(1)
	v_add_f32_e32 v3, v3, v32
	v_lshl_add_u64 v[6:7], s[14:15], 0, v[4:5]
	v_lshl_add_u64 v[4:5], s[2:3], 0, v[4:5]
	v_lshlrev_b64 v[0:1], 12, v[0:1]
	global_store_dword v[4:5], v3, off sc1
	v_or3_b32 v1, v1, 0, 0
	v_or3_b32 v0, v0, v36, s16
	s_waitcnt lgkmcnt(0)
	v_add_f32_e32 v4, v2, v33
	v_mul_f32_e32 v8, v11, v3
	v_mul_f32_e32 v5, v11, v4
	v_lshlrev_b64 v[0:1], 2, v[0:1]
	v_fmac_f32_e32 v8, v10, v45
	v_fmac_f32_e32 v5, v10, v43
	v_lshl_add_u64 v[2:3], s[14:15], 0, v[0:1]
	v_lshl_add_u64 v[0:1], s[2:3], 0, v[0:1]
	global_store_dword v[6:7], v8, off sc1
	global_store_dword v[2:3], v5, off sc1
	global_store_dword v[0:1], v4, off sc1
	s_endpgm
